# P11 row gather: saddr-form loads with a per-query SGPR base, 1 VALU per row address instead of 5 (three 64-bit)
# baseline (speedup 1.0000x reference)
.LBB0_1462:
	s_or_b64 exec, exec, s[2:3]
	s_ashr_i32 s19, s18, 31
	s_lshl_b64 s[2:3], s[16:17], 12
	s_add_u32 s44, s24, s2
	s_addc_u32 s45, s25, s3
	v_lshlrev_b32_e32 v0, 8, v163
	v_and_b32_e32 v2, -16, v154
	v_lshl_add_u64 v[8:9], s[44:45], 0, v[0:1]
	v_ashrrev_i32_e32 v3, 31, v2
	v_lshl_add_u64 v[20:21], v[8:9], 0, v[2:3]
	global_load_dwordx4 v[8:11], v[20:21], off nt
	global_load_dwordx4 v[12:15], v[20:21], off offset:64 nt
	global_load_dwordx4 v[16:19], v[20:21], off offset:128 nt
	s_nop 0
	global_load_dwordx4 v[20:23], v[20:21], off offset:192 nt
	s_waitcnt lgkmcnt(0)
	v_or_b32_e32 v0, v6, v4
	v_cmp_ge_i32_e32 vcc, s20, v163
	v_lshl_add_u32 v4, v154, 2, s31
	v_or3_b32 v0, v0, v5, v7
	v_cndmask_b32_e32 v5, 0, v163, vcc
	ds_write_b32 v4, v0
	v_lshl_add_u32 v0, v5, 1, s30
	s_waitcnt lgkmcnt(0)
	ds_read_u16 v0, v0
	s_lshl_b64 s[18:19], s[18:19], 13
	s_lshl_b64 s[50:51], s[18:19], 8
	s_add_u32 s50, s50, s4
	s_addc_u32 s51, s51, s5
	v_mov_b32_e32 v156, v2
	s_mov_b32 s17, 0
	v_or_b32_e32 v199, 64, v163
	v_mov_b32_e32 v200, 0xff800000
	v_mov_b32_e32 v185, 0
	s_waitcnt vmcnt(3)
	v_cvt_scalef32_pk_bf16_fp8 v66, v8, 1.0
	v_cvt_scalef32_pk_bf16_fp8 v67, v8, 1.0 op_sel:[1,0,0]
	v_cvt_scalef32_pk_bf16_fp8 v68, v9, 1.0
	v_cvt_scalef32_pk_bf16_fp8 v69, v9, 1.0 op_sel:[1,0,0]
	v_or_b32_e32 v4, 16, v163
	v_cmp_ge_i32_e32 vcc, s6, v4
	v_or_b32_e32 v5, 32, v163
	v_cndmask_b32_e32 v4, 0, v4, vcc
	v_cmp_ge_i32_e32 vcc, s6, v5
	v_lshl_add_u32 v4, v4, 1, s30
	v_lshlrev_b32_e32 v6, 2, v164
	v_cndmask_b32_e32 v5, 0, v5, vcc
	v_lshl_add_u32 v5, v5, 1, s30
	v_add_u32_e32 v195, s31, v6
	ds_read_u16 v7, v4
	ds_read_u16 v196, v5
	ds_read_b32 v197, v195
	s_waitcnt lgkmcnt(3)
	v_and_b32_e32 v4, 0xffff, v0
	v_mov_b32_e32 v5, s7
	v_lshl_add_u64 v[4:5], s[18:19], 0, v[4:5]
	v_lshlrev_b64 v[4:5], 8, v[4:5]
	v_lshl_add_u64 v[4:5], s[4:5], 0, v[4:5]
	v_lshl_add_u64 v[4:5], v[4:5], 0, v[2:3]
	global_load_dwordx4 v[110:113], v[4:5], off
	global_load_dwordx4 v[106:109], v[4:5], off offset:64
	global_load_dwordx4 v[102:105], v[4:5], off offset:128
	global_load_dwordx4 v[98:101], v[4:5], off offset:192
	s_waitcnt lgkmcnt(2)
	v_and_b32_e32 v4, 0xffff, v7
	v_mov_b32_e32 v5, s7
	v_lshl_add_u64 v[4:5], s[18:19], 0, v[4:5]
	v_lshlrev_b64 v[4:5], 8, v[4:5]
	v_lshl_add_u64 v[4:5], s[4:5], 0, v[4:5]
	v_lshl_add_u64 v[4:5], v[4:5], 0, v[2:3]
	global_load_dwordx4 v[244:247], v[4:5], off
	global_load_dwordx4 v[240:243], v[4:5], off offset:64
	global_load_dwordx4 v[236:239], v[4:5], off offset:128
	global_load_dwordx4 v[232:235], v[4:5], off offset:192
	v_cvt_scalef32_pk_bf16_fp8 v82, v10, 1.0
	v_cvt_scalef32_pk_bf16_fp8 v83, v10, 1.0 op_sel:[1,0,0]
	v_cvt_scalef32_pk_bf16_fp8 v84, v11, 1.0
	v_cvt_scalef32_pk_bf16_fp8 v85, v11, 1.0 op_sel:[1,0,0]
	s_waitcnt vmcnt(10)
	v_cvt_scalef32_pk_bf16_fp8 v70, v12, 1.0
	v_cvt_scalef32_pk_bf16_fp8 v71, v12, 1.0 op_sel:[1,0,0]
	v_cvt_scalef32_pk_bf16_fp8 v72, v13, 1.0
	v_cvt_scalef32_pk_bf16_fp8 v73, v13, 1.0 op_sel:[1,0,0]
	v_cvt_scalef32_pk_bf16_fp8 v86, v14, 1.0
	v_cvt_scalef32_pk_bf16_fp8 v87, v14, 1.0 op_sel:[1,0,0]
	v_cvt_scalef32_pk_bf16_fp8 v88, v15, 1.0
	v_cvt_scalef32_pk_bf16_fp8 v89, v15, 1.0 op_sel:[1,0,0]
	s_waitcnt vmcnt(9)
	v_cvt_scalef32_pk_bf16_fp8 v74, v16, 1.0
	v_cvt_scalef32_pk_bf16_fp8 v75, v16, 1.0 op_sel:[1,0,0]
	v_cvt_scalef32_pk_bf16_fp8 v76, v17, 1.0
	v_cvt_scalef32_pk_bf16_fp8 v77, v17, 1.0 op_sel:[1,0,0]
	v_cvt_scalef32_pk_bf16_fp8 v90, v18, 1.0
	v_cvt_scalef32_pk_bf16_fp8 v91, v18, 1.0 op_sel:[1,0,0]
	v_cvt_scalef32_pk_bf16_fp8 v92, v19, 1.0
	v_cvt_scalef32_pk_bf16_fp8 v93, v19, 1.0 op_sel:[1,0,0]
	s_waitcnt vmcnt(8)
	v_cvt_scalef32_pk_bf16_fp8 v78, v20, 1.0
	v_cvt_scalef32_pk_bf16_fp8 v79, v20, 1.0 op_sel:[1,0,0]
	v_cvt_scalef32_pk_bf16_fp8 v80, v21, 1.0
	v_cvt_scalef32_pk_bf16_fp8 v81, v21, 1.0 op_sel:[1,0,0]
	v_cvt_scalef32_pk_bf16_fp8 v94, v22, 1.0
	v_cvt_scalef32_pk_bf16_fp8 v95, v22, 1.0 op_sel:[1,0,0]
	v_cvt_scalef32_pk_bf16_fp8 v96, v23, 1.0
	v_cvt_pk_f32_fp8_sdwa v[22:23], v23 src0_sel:WORD_1
	v_mov_b32_e32 v2, v1
	v_mov_b32_e32 v3, v1
	v_cvt_pk_bf16_f32 v97, v22, v23
	v_add_u32_e32 v198, s37, v6
	v_mov_b32_e32 v0, v1
	v_mov_b64_e32 v[64:65], v[2:3]
	v_mov_b64_e32 v[60:61], v[2:3]
	v_mov_b64_e32 v[56:57], v[2:3]
	v_mov_b64_e32 v[52:53], v[2:3]
	v_mov_b64_e32 v[48:49], v[2:3]
	v_mov_b64_e32 v[44:45], v[2:3]
	v_mov_b64_e32 v[40:41], v[2:3]
	v_mov_b64_e32 v[36:37], v[2:3]
	v_mov_b64_e32 v[32:33], v[2:3]
	v_mov_b64_e32 v[28:29], v[2:3]
	v_mov_b64_e32 v[24:25], v[2:3]
	v_mov_b64_e32 v[20:21], v[2:3]
	v_mov_b64_e32 v[16:17], v[2:3]
	v_mov_b64_e32 v[12:13], v[2:3]
	v_mov_b64_e32 v[8:9], v[2:3]
	v_mov_b64_e32 v[62:63], v[0:1]
	v_mov_b64_e32 v[58:59], v[0:1]
	v_mov_b64_e32 v[54:55], v[0:1]
	v_mov_b64_e32 v[50:51], v[0:1]
	v_mov_b64_e32 v[46:47], v[0:1]
	v_mov_b64_e32 v[42:43], v[0:1]
	v_mov_b64_e32 v[38:39], v[0:1]
	v_mov_b64_e32 v[34:35], v[0:1]
	v_mov_b64_e32 v[30:31], v[0:1]
	v_mov_b64_e32 v[26:27], v[0:1]
	v_mov_b64_e32 v[22:23], v[0:1]
	v_mov_b64_e32 v[18:19], v[0:1]
	v_mov_b64_e32 v[14:15], v[0:1]
	v_mov_b64_e32 v[10:11], v[0:1]
	v_mov_b64_e32 v[6:7], v[0:1]
	v_mov_b64_e32 v[4:5], v[2:3]
	v_mov_b64_e32 v[2:3], v[0:1]
.LBB0_1463:
	s_waitcnt lgkmcnt(0)
	v_lshlrev_b32_e32 v0, 6, v197
	v_and_b32_e32 v0, 0x3fc0, v0
	v_add_u32_e32 v0, v189, v0
	v_bfe_u32 v114, v197, 8, 8
	v_bfe_u32 v115, v197, 16, 8
	v_lshrrev_b32_e32 v116, 24, v197
	ds_read_b32 v220, v198
	v_lshl_add_u32 v114, v114, 6, v189
	v_lshl_add_u32 v115, v115, 6, v189
	v_lshl_add_u32 v116, v116, 6, v189
	ds_read_b32 v0, v0
	ds_read_b32 v201, v114
	ds_read_b32 v202, v115
	ds_read_b32 v203, v116
	s_waitcnt vmcnt(7)
	v_cvt_scalef32_pk_bf16_fp8 v114, v110, 1.0
	v_cvt_scalef32_pk_bf16_fp8 v115, v110, 1.0 op_sel:[1,0,0]
	v_cvt_scalef32_pk_bf16_fp8 v116, v111, 1.0
	v_cvt_scalef32_pk_bf16_fp8 v117, v111, 1.0 op_sel:[1,0,0]
	v_cvt_scalef32_pk_bf16_fp8 v118, v112, 1.0
	v_cvt_scalef32_pk_bf16_fp8 v119, v112, 1.0 op_sel:[1,0,0]
	v_cvt_scalef32_pk_bf16_fp8 v120, v113, 1.0
	v_cvt_scalef32_pk_bf16_fp8 v121, v113, 1.0 op_sel:[1,0,0]
	s_waitcnt vmcnt(6)
	v_cvt_scalef32_pk_bf16_fp8 v122, v106, 1.0
	v_cvt_scalef32_pk_bf16_fp8 v123, v106, 1.0 op_sel:[1,0,0]
	v_cvt_scalef32_pk_bf16_fp8 v124, v107, 1.0
	v_cvt_scalef32_pk_bf16_fp8 v125, v107, 1.0 op_sel:[1,0,0]
	v_cvt_scalef32_pk_bf16_fp8 v126, v108, 1.0
	v_cvt_scalef32_pk_bf16_fp8 v127, v108, 1.0 op_sel:[1,0,0]
	v_cvt_scalef32_pk_bf16_fp8 v128, v109, 1.0
	v_cvt_scalef32_pk_bf16_fp8 v129, v109, 1.0 op_sel:[1,0,0]
	s_waitcnt vmcnt(5)
	v_cvt_scalef32_pk_bf16_fp8 v146, v102, 1.0
	v_cvt_scalef32_pk_bf16_fp8 v147, v102, 1.0 op_sel:[1,0,0]
	v_cvt_scalef32_pk_bf16_fp8 v148, v103, 1.0
	v_cvt_scalef32_pk_bf16_fp8 v149, v103, 1.0 op_sel:[1,0,0]
	v_cvt_scalef32_pk_bf16_fp8 v150, v104, 1.0
	v_cvt_scalef32_pk_bf16_fp8 v151, v104, 1.0 op_sel:[1,0,0]
	v_cvt_scalef32_pk_bf16_fp8 v152, v105, 1.0
	v_cvt_scalef32_pk_bf16_fp8 v153, v105, 1.0 op_sel:[1,0,0]
	s_waitcnt vmcnt(4)
	v_cvt_scalef32_pk_bf16_fp8 v204, v98, 1.0
	v_cvt_scalef32_pk_bf16_fp8 v205, v98, 1.0 op_sel:[1,0,0]
	v_cvt_scalef32_pk_bf16_fp8 v206, v99, 1.0
	v_cvt_scalef32_pk_bf16_fp8 v207, v99, 1.0 op_sel:[1,0,0]
	v_cvt_scalef32_pk_bf16_fp8 v208, v100, 1.0
	v_cvt_scalef32_pk_bf16_fp8 v209, v100, 1.0 op_sel:[1,0,0]
	v_cvt_scalef32_pk_bf16_fp8 v210, v101, 1.0
	v_cvt_scalef32_pk_bf16_fp8 v211, v101, 1.0 op_sel:[1,0,0]
	v_lshl_add_u32 v98, v196, 8, v156
	global_load_dwordx4 v[110:113], v98, s[50:51]
	global_load_dwordx4 v[106:109], v98, s[50:51] offset:64
	global_load_dwordx4 v[102:105], v98, s[50:51] offset:128
	s_nop 0
	global_load_dwordx4 v[98:101], v98, s[50:51] offset:192
	v_mfma_f32_16x16x32_bf16 v[212:215], v[114:117], v[66:69], 0
	v_add_u32_e32 v196, -16, v199
	v_cmp_ge_i32_e32 vcc, s6, v196
	v_mfma_f32_16x16x32_bf16 v[212:215], v[122:125], v[70:73], v[212:215]
	s_nop 0
	v_cndmask_b32_e32 v196, 0, v196, vcc
	v_lshl_add_u32 v196, v196, 1, s30
	ds_read_u16 v196, v196
	v_mfma_f32_16x16x32_bf16 v[216:219], v[118:121], v[82:85], 0
	ds_write_b128 v193, v[114:117]
	ds_write_b128 v194, v[118:121]
	ds_write_b128 v190, v[122:125]
	ds_write_b128 v191, v[126:129]
	ds_write_b128 v192, v[146:149]
	ds_write_b128 v186, v[150:153]
	ds_write_b128 v187, v[204:207]
	ds_write_b128 v188, v[208:211]
	v_mfma_f32_16x16x32_bf16 v[114:117], v[146:149], v[74:77], v[212:215]
	ds_read_b32 v197, v198 offset:16
	v_mfma_f32_16x16x32_bf16 v[216:219], v[126:129], v[86:89], v[216:219]
	v_mfma_f32_16x16x32_bf16 v[146:149], v[204:207], v[78:81], v[114:117]
	s_waitcnt lgkmcnt(14)
	s_nop 3
	v_lshlrev_b32_e32 v114, 6, v220
	v_and_b32_e32 v114, 0x3fc0, v114
	v_mfma_f32_16x16x32_bf16 v[118:121], v[150:153], v[90:93], v[216:219]
	v_add_u32_e32 v114, v189, v114
	v_bfe_u32 v115, v220, 8, 8
	v_bfe_u32 v116, v220, 16, 8
	v_lshrrev_b32_e32 v117, 24, v220
	v_lshl_add_u32 v115, v115, 6, v189
	v_lshl_add_u32 v116, v116, 6, v189
	v_lshl_add_u32 v117, v117, 6, v189
	ds_read_b32 v204, v114
	ds_read_b32 v205, v115
	ds_read_b32 v206, v116
	ds_read_b32 v207, v117
	v_mfma_f32_16x16x32_bf16 v[150:153], v[208:211], v[94:97], v[118:121]
	s_waitcnt lgkmcnt(13)
	v_lshl_add_u32 v248, v196, 8, v156
	s_cmp_gt_u32 s17, 11
	s_cselect_b64 s[20:21], -1, 0
	s_and_b64 vcc, exec, s[20:21]
	s_cbranch_vccnz .LBB0_1465
	v_cmp_ge_i32_e32 vcc, s6, v199
	s_nop 1
	v_cndmask_b32_e32 v196, 0, v199, vcc
	v_lshl_add_u32 v196, v196, 1, s30
	ds_read_u16 v196, v196
.LBB0_1465:
	v_pk_add_f32 v[148:149], v[148:149], v[152:153]
	v_pk_add_f32 v[146:147], v[146:147], v[150:151]
	v_pk_mul_f32 v[150:151], v[148:149], s[14:15] op_sel_hi:[1,0]
	v_pk_mul_f32 v[146:147], v[146:147], s[14:15] op_sel_hi:[1,0]
	s_waitcnt vmcnt(7)
	v_cvt_scalef32_pk_bf16_fp8 v152, v245, 1.0
	v_add_f32_e32 v149, v0, v146
	v_add_f32_e32 v148, v201, v147
	v_add_f32_e32 v147, v202, v150
	v_add_f32_e32 v146, v203, v151
	v_cvt_scalef32_pk_bf16_fp8 v150, v244, 1.0
	v_cvt_scalef32_pk_bf16_fp8 v151, v244, 1.0 op_sel:[1,0,0]
	v_cvt_scalef32_pk_bf16_fp8 v153, v245, 1.0 op_sel:[1,0,0]
	v_cvt_scalef32_pk_bf16_fp8 v142, v246, 1.0
	v_cvt_scalef32_pk_bf16_fp8 v143, v246, 1.0 op_sel:[1,0,0]
	v_cvt_scalef32_pk_bf16_fp8 v144, v247, 1.0
	v_cvt_scalef32_pk_bf16_fp8 v145, v247, 1.0 op_sel:[1,0,0]
	s_waitcnt vmcnt(6)
	v_cvt_scalef32_pk_bf16_fp8 v208, v240, 1.0
	v_cvt_scalef32_pk_bf16_fp8 v209, v240, 1.0 op_sel:[1,0,0]
	v_cvt_scalef32_pk_bf16_fp8 v210, v241, 1.0
	v_cvt_scalef32_pk_bf16_fp8 v211, v241, 1.0 op_sel:[1,0,0]
	v_cvt_scalef32_pk_bf16_fp8 v138, v242, 1.0
	v_cvt_scalef32_pk_bf16_fp8 v139, v242, 1.0 op_sel:[1,0,0]
	v_cvt_scalef32_pk_bf16_fp8 v140, v243, 1.0
	v_cvt_scalef32_pk_bf16_fp8 v141, v243, 1.0 op_sel:[1,0,0]
	v_mfma_f32_16x16x32_bf16 v[212:215], v[150:153], v[66:69], 0
	s_waitcnt vmcnt(5)
	v_cvt_scalef32_pk_bf16_fp8 v216, v236, 1.0
	v_cvt_scalef32_pk_bf16_fp8 v217, v236, 1.0 op_sel:[1,0,0]
	v_cvt_scalef32_pk_bf16_fp8 v218, v237, 1.0
	v_mfma_f32_16x16x32_bf16 v[220:223], v[142:145], v[82:85], 0
	v_cvt_scalef32_pk_bf16_fp8 v219, v237, 1.0 op_sel:[1,0,0]
	v_cvt_scalef32_pk_bf16_fp8 v224, v238, 1.0
	v_cvt_scalef32_pk_bf16_fp8 v225, v238, 1.0 op_sel:[1,0,0]
	v_cvt_scalef32_pk_bf16_fp8 v226, v239, 1.0
	v_cvt_scalef32_pk_bf16_fp8 v227, v239, 1.0 op_sel:[1,0,0]
	v_mfma_f32_16x16x32_bf16 v[212:215], v[208:211], v[70:73], v[212:215]
	s_waitcnt vmcnt(4)
	v_cvt_scalef32_pk_bf16_fp8 v228, v232, 1.0
	v_cvt_scalef32_pk_bf16_fp8 v229, v232, 1.0 op_sel:[1,0,0]
	v_cvt_scalef32_pk_bf16_fp8 v230, v233, 1.0
	v_mfma_f32_16x16x32_bf16 v[134:137], v[138:141], v[86:89], v[220:223]
	v_cvt_scalef32_pk_bf16_fp8 v231, v233, 1.0 op_sel:[1,0,0]
	v_max_f32_e32 v0, v149, v148
	ds_write_b128 v193, v[150:153] offset:8192
	ds_write_b128 v194, v[142:145] offset:8192
	v_cvt_scalef32_pk_bf16_fp8 v220, v234, 1.0
	v_cvt_scalef32_pk_bf16_fp8 v221, v234, 1.0 op_sel:[1,0,0]
	v_cvt_scalef32_pk_bf16_fp8 v222, v235, 1.0
	v_cvt_scalef32_pk_bf16_fp8 v223, v235, 1.0 op_sel:[1,0,0]
	global_load_dwordx4 v[244:247], v248, s[50:51]
	global_load_dwordx4 v[240:243], v248, s[50:51] offset:64
	global_load_dwordx4 v[236:239], v248, s[50:51] offset:128
	global_load_dwordx4 v[232:235], v248, s[50:51] offset:192
	v_mfma_f32_16x16x32_bf16 v[212:215], v[216:219], v[74:77], v[212:215]
	ds_write_b128 v190, v[208:211] offset:8192
	ds_write_b128 v191, v[138:141] offset:8192
	ds_write_b128 v192, v[216:219] offset:8192
	ds_write_b128 v186, v[224:227] offset:8192
	ds_write_b128 v187, v[228:231] offset:8192
	ds_write_b128 v188, v[220:223] offset:8192
	v_mfma_f32_16x16x32_bf16 v[134:137], v[224:227], v[90:93], v[134:137]
	v_mfma_f32_16x16x32_bf16 v[130:133], v[228:231], v[78:81], v[212:215]
	v_mfma_f32_16x16x32_bf16 v[134:137], v[220:223], v[94:97], v[134:137]
	s_nop 7
	v_pk_add_f32 v[132:133], v[132:133], v[136:137]
	v_pk_add_f32 v[130:131], v[130:131], v[134:135]
	v_pk_mul_f32 v[134:135], v[132:133], s[14:15] op_sel_hi:[1,0]
	v_pk_mul_f32 v[130:131], v[130:131], s[14:15] op_sel_hi:[1,0]
	s_waitcnt lgkmcnt(11)
	v_add_f32_e32 v133, v204, v130
	s_waitcnt lgkmcnt(10)
	v_add_f32_e32 v132, v205, v131
	s_waitcnt lgkmcnt(9)
	v_add_f32_e32 v131, v206, v134
	s_waitcnt lgkmcnt(8)
	v_add_f32_e32 v130, v207, v135
	v_max_f32_e32 v135, v131, v130
	v_max_f32_e32 v134, v147, v146
	v_max3_f32 v135, v133, v132, v135
	v_max3_f32 v0, v0, v134, v135
	v_mov_b32_e32 v134, v0
	s_nop 1
	v_permlane16_swap_b32_e32 v0, v134
	v_max_f32_e32 v134, v134, v134
	v_max_f32_e32 v0, v0, v0
	v_max_f32_e32 v0, v0, v134
	v_mov_b32_e32 v134, v0
	s_nop 1
	v_permlane32_swap_b32_e32 v0, v134
	v_max_f32_e32 v134, v134, v134
	v_max_f32_e32 v0, v0, v0
	v_max_f32_e32 v0, v0, v134
	v_add_f32_e32 v134, 0x41000000, v200
	v_cmp_gt_f32_e32 vcc, v0, v134
	s_nop 1
	v_cndmask_b32_e32 v0, v200, v0, vcc
	v_sub_f32_e32 v134, v200, v0
	v_exp_f32_e32 v134, v134
	s_nop 0
	v_cmp_neq_f32_e32 vcc, 1.0, v134
	s_cbranch_vccz .LBB0_1467
	ds_bpermute_b32 v136, v167, v134
	ds_bpermute_b32 v138, v165, v134
	ds_bpermute_b32 v139, v166, v134
	ds_bpermute_b32 v137, v168, v134
	s_waitcnt lgkmcnt(1)
	v_pk_mul_f32 v[64:65], v[64:65], v[138:139]
	s_waitcnt lgkmcnt(0)
	v_pk_mul_f32 v[62:63], v[62:63], v[136:137]
	v_pk_mul_f32 v[60:61], v[60:61], v[138:139]
	v_pk_mul_f32 v[58:59], v[58:59], v[136:137]
	v_pk_mul_f32 v[56:57], v[56:57], v[138:139]
	v_pk_mul_f32 v[54:55], v[54:55], v[136:137]
	v_pk_mul_f32 v[52:53], v[52:53], v[138:139]
	v_pk_mul_f32 v[50:51], v[50:51], v[136:137]
	v_pk_mul_f32 v[48:49], v[48:49], v[138:139]
	v_pk_mul_f32 v[46:47], v[46:47], v[136:137]
	v_pk_mul_f32 v[44:45], v[44:45], v[138:139]
	v_pk_mul_f32 v[42:43], v[42:43], v[136:137]
	v_pk_mul_f32 v[40:41], v[40:41], v[138:139]
	v_pk_mul_f32 v[38:39], v[38:39], v[136:137]
	v_pk_mul_f32 v[36:37], v[36:37], v[138:139]
	v_pk_mul_f32 v[34:35], v[34:35], v[136:137]
	v_pk_mul_f32 v[32:33], v[32:33], v[138:139]
	v_pk_mul_f32 v[30:31], v[30:31], v[136:137]
	v_pk_mul_f32 v[28:29], v[28:29], v[138:139]
	v_pk_mul_f32 v[26:27], v[26:27], v[136:137]
	v_pk_mul_f32 v[24:25], v[24:25], v[138:139]
	v_pk_mul_f32 v[22:23], v[22:23], v[136:137]
	v_pk_mul_f32 v[20:21], v[20:21], v[138:139]
	v_pk_mul_f32 v[18:19], v[18:19], v[136:137]
	v_pk_mul_f32 v[16:17], v[16:17], v[138:139]
	v_pk_mul_f32 v[14:15], v[14:15], v[136:137]
	v_pk_mul_f32 v[12:13], v[12:13], v[138:139]
	v_pk_mul_f32 v[10:11], v[10:11], v[136:137]
	v_pk_mul_f32 v[8:9], v[8:9], v[138:139]
	v_pk_mul_f32 v[6:7], v[6:7], v[136:137]
	v_pk_mul_f32 v[4:5], v[4:5], v[138:139]
	v_pk_mul_f32 v[2:3], v[2:3], v[136:137]
